# gMLP gating epilogue (both layers): in-quad transpose, 12 wide loads issued together, 8 dwordx2 stores per lane instead of 48 narrow loads + 32 short stores in a serial chain (1)
# speedup vs baseline: 1.0155x; 1.0113x over previous
; #define LAS __attribute__((address_space(3)))
; __device__ __forceinline__ bf16_t f2bf(float f) { return (bf16_t)(cvt_pk_bf16(f, 0.f) & 0xffffu); }
; __device__ __forceinline__ void unpack8(u32x4 w, f32x4& v0, f32x4& v1) { v0 = (f32x4){bf_lo(w.x), bf_hi(w.x), bf_lo(w.y), bf_hi(w.y)}; v1 = (f32x4){bf_lo(w.z), bf_hi(w.z), bf_lo(w.w), bf_hi(w.w)}; }
; __device__ __forceinline__ float ss_val(const ss_t* ss, int row) { return (float)ss[row] * (1.f / 16777216.f); }
; __device__ __forceinline__ void gmlp_item(const bf16_t* __restrict__ proj, const epi::ss_t* __restrict__ ssv, const float* __restrict__ vgain, const bf16_t* __restrict__ wsb_l, const float* __restrict__ bs_l, ...
;     ...
;     { const int p = tid >> 2, cb = (tid & 3) * 32; const float rs = rsqrtf(epi::ss_val(ssv, tok0 + p) * (1.f / 1024.f) + EPS);
; #pragma unroll
;       for (int cc = 0; cc < 4; ++cc) { const int c0 = cb + cc * 8; f32x4 v0, v1; epi::unpack8(*(const u32x4*)(proj + (size_t)(tok0 + p) * NIN + C_ZV + g * 128 + c0), v0, v1);
;           const f32x4 g0 = *(const f32x4*)(vgain + g * 128 + c0), g1 = *(const f32x4*)(vgain + g * 128 + c0 + 4);
; #pragma unroll
;           for (int i = 0; i < 4; ++i) { *(LAS bf16_t*)(lds + ((c0 + i) * 136 + p) * 2) = f2bf(v0[i] * rs * g0[i]); *(LAS bf16_t*)(lds + ((c0 + 4 + i) * 136 + p) * 2) = f2bf(v1[i] * rs * g1[i]); } } }
;     __syncthreads();
.LBB0_651:
	s_and_b32 s17, s3, 0xffffff80
	v_or_b32_e32 v4, s17, v46
	v_mov_b64_e32 v[40:41], s[60:61]
	v_ashrrev_i32_e32 v5, 31, v4
	v_mad_i64_i32 v[6:7], s[22:23], v4, s14, v[40:41]
	v_lshl_add_u64 v[4:5], v[4:5], 3, s[66:67]
	global_load_dwordx2 v[14:15], v[4:5], off
	s_and_b32 s20, s11, 0x380
	s_lshl_b32 s0, s20, 1
	v_or_b32_e32 v2, s20, v47
	v_mov_b32_e32 v3, v35
	v_lshlrev_b32_e32 v2, 8, v2
	v_lshl_add_u64 v[6:7], v[6:7], 0, s[0:1]
	v_lshl_add_u64 v[44:45], v[36:37], 0, v[2:3]
	v_lshl_add_u64 v[2:3], v[6:7], 0, v[34:35]
	s_lshl_b32 s0, s20, 2
	v_add_co_u32_e32 v10, vcc, s15, v2
	v_lshl_add_u64 v[16:17], v[38:39], 0, s[0:1]
	s_nop 0
	v_addc_co_u32_e32 v11, vcc, 0, v3, vcc
	v_lshl_add_u64 v[18:19], v[2:3], 0, s[4:5]
	global_load_dwordx4 v[2:5], v[16:17], off offset:16
	global_load_dwordx4 v[6:9], v[16:17], off
	s_nop 0
	global_load_dwordx4 v[10:13], v[10:11], off offset:3072
	v_or_b32_e32 v42, s20, v48
	v_or_b32_e32 v120, s17, v49
	v_mov_b32_e32 v43, v35
	v_or_b32_e32 v99, s20, v49
	v_lshlrev_b32_e32 v42, 1, v42
	v_lshlrev_b32_e32 v99, 2, v99
	s_add_i32 s16, s16, s33
	s_add_i32 s3, s3, s10
	s_add_i32 s11, s11, s12
	s_cmpk_lt_i32 s16, 0x200
	s_waitcnt vmcnt(3)
	v_ffbh_u32_e32 v20, v15
	v_min_u32_e32 v20, 32, v20
	v_lshlrev_b64 v[14:15], v20, v[14:15]
	v_min_u32_e32 v14, 1, v14
	v_or_b32_e32 v14, v15, v14
	v_cvt_f32_u32_e32 v14, v14
	v_sub_u32_e32 v20, 32, v20
	v_ldexp_f32 v14, v14, v20
	v_mul_f32_e32 v14, 0x33800000, v14
	v_fmamk_f32 v14, v14, 0x3a800000, v65
	v_mul_f32_e32 v15, 0x4b800000, v14
	v_cmp_gt_f32_e32 vcc, s13, v14
	s_waitcnt vmcnt(0)
	v_lshlrev_b32_e32 v21, 16, v10
	v_cndmask_b32_e32 v14, v14, v15, vcc
	v_rsq_f32_e32 v14, v14
	v_lshlrev_b32_e32 v23, 16, v12
	v_and_b32_e32 v10, 0xffff0000, v10
	v_and_b32_e32 v12, 0xffff0000, v12
	v_mul_f32_e32 v15, 0x45800000, v14
	v_cndmask_b32_e32 v14, v14, v15, vcc
	v_mul_f32_e32 v15, v14, v21
	v_mul_f32_e32 v20, v14, v23
	v_mul_f32_e32 v6, v6, v15
	v_mul_f32_e32 v2, v2, v20
	v_mul_f32_e32 v10, v14, v10
	v_cvt_pk_bf16_f32 v6, v6, v35
	ds_write_b16 v66, v6
	v_cvt_pk_bf16_f32 v2, v2, v35
	v_lshlrev_b32_e32 v22, 16, v11
	v_mul_f32_e32 v12, v14, v12
	v_mul_f32_e32 v7, v7, v10
	ds_write_b16 v67, v2
	v_cvt_pk_bf16_f32 v2, v7, v35
	v_lshlrev_b32_e32 v24, 16, v13
	v_mul_f32_e32 v21, v14, v22
	v_mul_f32_e32 v3, v3, v12
	ds_write_b16 v68, v2
	v_cvt_pk_bf16_f32 v2, v3, v35
	v_and_b32_e32 v11, 0xffff0000, v11
	v_and_b32_e32 v13, 0xffff0000, v13
	v_mul_f32_e32 v22, v14, v24
	v_mul_f32_e32 v8, v8, v21
	ds_write_b16 v69, v2
	v_cvt_pk_bf16_f32 v2, v8, v35
	v_mul_f32_e32 v11, v14, v11
	v_mul_f32_e32 v13, v14, v13
	v_mul_f32_e32 v4, v4, v22
	ds_write_b16 v70, v2
	v_cvt_pk_bf16_f32 v2, v4, v35
	v_mul_f32_e32 v9, v9, v11
	v_mul_f32_e32 v5, v5, v13
	ds_write_b16 v71, v2
	v_cvt_pk_bf16_f32 v2, v9, v35
	ds_write_b16 v72, v2
	v_cvt_pk_bf16_f32 v15, v5, v35
	global_load_dwordx4 v[2:5], v[18:19], off offset:16
	global_load_dwordx4 v[6:9], v[16:17], off offset:32
	global_load_dwordx4 v[10:13], v[16:17], off offset:48
	ds_write_b16 v73, v15
	s_waitcnt vmcnt(2)
	v_lshlrev_b32_e32 v15, 16, v2
	v_and_b32_e32 v2, 0xffff0000, v2
	v_mul_f32_e32 v15, v14, v15
	v_lshlrev_b32_e32 v21, 16, v4
	v_mul_f32_e32 v2, v14, v2
	s_waitcnt vmcnt(1)
	v_mul_f32_e32 v6, v6, v15
	v_and_b32_e32 v4, 0xffff0000, v4
	v_mul_f32_e32 v21, v14, v21
	v_mul_f32_e32 v2, v7, v2
	v_cvt_pk_bf16_f32 v6, v6, v35
	v_lshlrev_b32_e32 v20, 16, v3
	v_mul_f32_e32 v4, v14, v4
	s_waitcnt vmcnt(0)
	v_mul_f32_e32 v10, v10, v21
	ds_write_b16 v74, v6
	v_cvt_pk_bf16_f32 v6, v10, v35
	ds_write_b16 v75, v6
	v_cvt_pk_bf16_f32 v2, v2, v35
	v_lshlrev_b32_e32 v22, 16, v5
	v_mul_f32_e32 v20, v14, v20
	v_mul_f32_e32 v4, v11, v4
	ds_write_b16 v76, v2
	v_cvt_pk_bf16_f32 v2, v4, v35
	v_and_b32_e32 v3, 0xffff0000, v3
	v_and_b32_e32 v5, 0xffff0000, v5
	v_mul_f32_e32 v22, v14, v22
	v_mul_f32_e32 v7, v8, v20
	ds_write_b16 v77, v2
	v_cvt_pk_bf16_f32 v2, v7, v35
	v_mul_f32_e32 v3, v14, v3
	v_mul_f32_e32 v5, v14, v5
	v_mul_f32_e32 v8, v12, v22
	ds_write_b16 v78, v2
	v_cvt_pk_bf16_f32 v2, v8, v35
	v_mul_f32_e32 v3, v9, v3
	v_mul_f32_e32 v5, v13, v5
	ds_write_b16 v79, v2
	v_cvt_pk_bf16_f32 v2, v3, v35
	ds_write_b16 v80, v2
	v_cvt_pk_bf16_f32 v15, v5, v35
	global_load_dwordx4 v[2:5], v[18:19], off offset:32
	global_load_dwordx4 v[6:9], v[16:17], off offset:64
	global_load_dwordx4 v[10:13], v[16:17], off offset:80
	ds_write_b16 v81, v15
	s_waitcnt vmcnt(2)
	v_lshlrev_b32_e32 v15, 16, v2
	v_and_b32_e32 v2, 0xffff0000, v2
	v_mul_f32_e32 v15, v14, v15
	v_lshlrev_b32_e32 v21, 16, v4
	v_mul_f32_e32 v2, v14, v2
	s_waitcnt vmcnt(1)
	v_mul_f32_e32 v6, v6, v15
	v_and_b32_e32 v4, 0xffff0000, v4
	v_mul_f32_e32 v21, v14, v21
	v_mul_f32_e32 v2, v7, v2
	v_cvt_pk_bf16_f32 v6, v6, v35
	v_lshlrev_b32_e32 v20, 16, v3
	v_mul_f32_e32 v4, v14, v4
	s_waitcnt vmcnt(0)
	v_mul_f32_e32 v10, v10, v21
	ds_write_b16 v82, v6
	v_cvt_pk_bf16_f32 v6, v10, v35
	ds_write_b16 v83, v6
	v_cvt_pk_bf16_f32 v2, v2, v35
	v_lshlrev_b32_e32 v22, 16, v5
	v_mul_f32_e32 v20, v14, v20
	v_mul_f32_e32 v4, v11, v4
	ds_write_b16 v84, v2
	v_cvt_pk_bf16_f32 v2, v4, v35
	v_and_b32_e32 v3, 0xffff0000, v3
	v_and_b32_e32 v5, 0xffff0000, v5
	v_mul_f32_e32 v22, v14, v22
	v_mul_f32_e32 v7, v8, v20
	ds_write_b16 v85, v2
	v_cvt_pk_bf16_f32 v2, v7, v35
	v_mul_f32_e32 v3, v14, v3
	v_mul_f32_e32 v5, v14, v5
	v_mul_f32_e32 v8, v12, v22
	ds_write_b16 v86, v2
	v_cvt_pk_bf16_f32 v2, v8, v35
	v_mul_f32_e32 v3, v9, v3
	v_mul_f32_e32 v5, v13, v5
	ds_write_b16 v87, v2
	v_cvt_pk_bf16_f32 v2, v3, v35
	ds_write_b16 v88, v2
	v_cvt_pk_bf16_f32 v15, v5, v35
	global_load_dwordx4 v[2:5], v[18:19], off offset:48
	global_load_dwordx4 v[6:9], v[16:17], off offset:96
	global_load_dwordx4 v[10:13], v[16:17], off offset:112
	ds_write_b16 v89, v15
	s_waitcnt vmcnt(2)
	v_lshlrev_b32_e32 v15, 16, v2
	v_and_b32_e32 v2, 0xffff0000, v2
	v_mul_f32_e32 v15, v14, v15
	v_lshlrev_b32_e32 v17, 16, v4
	v_mul_f32_e32 v2, v14, v2
	s_waitcnt vmcnt(1)
	v_mul_f32_e32 v6, v6, v15
	v_and_b32_e32 v4, 0xffff0000, v4
	v_mul_f32_e32 v17, v14, v17
	v_mul_f32_e32 v2, v7, v2
	v_cvt_pk_bf16_f32 v6, v6, v35
	v_lshlrev_b32_e32 v16, 16, v3
	v_mul_f32_e32 v4, v14, v4
	s_waitcnt vmcnt(0)
	v_mul_f32_e32 v10, v10, v17
	ds_write_b16 v90, v6
	v_cvt_pk_bf16_f32 v6, v10, v35
	ds_write_b16 v91, v6
	v_cvt_pk_bf16_f32 v2, v2, v35
	v_lshlrev_b32_e32 v18, 16, v5
	v_mul_f32_e32 v16, v14, v16
	v_mul_f32_e32 v4, v11, v4
	ds_write_b16 v92, v2
	v_cvt_pk_bf16_f32 v2, v4, v35
	v_and_b32_e32 v3, 0xffff0000, v3
	v_mul_f32_e32 v18, v14, v18
	v_mul_f32_e32 v7, v8, v16
	ds_write_b16 v93, v2
	v_cvt_pk_bf16_f32 v2, v7, v35
	v_and_b32_e32 v5, 0xffff0000, v5
	v_mul_f32_e32 v3, v14, v3
	v_mul_f32_e32 v8, v12, v18
	ds_write_b16 v94, v2
	v_cvt_pk_bf16_f32 v2, v8, v35
	v_mul_f32_e32 v5, v14, v5
	v_mul_f32_e32 v3, v9, v3
	ds_write_b16 v95, v2
	v_cvt_pk_bf16_f32 v2, v3, v35
	v_mul_f32_e32 v5, v13, v5
	ds_write_b16 v96, v2
	v_cvt_pk_bf16_f32 v2, v5, v35
	ds_write_b16 v97, v2
	s_waitcnt lgkmcnt(0)
	s_barrier
; #define LAS __attribute__((address_space(3)))
; __device__ __forceinline__ float bf2f(bf16_t b) { return __uint_as_float((unsigned)b << 16); }
; __device__ __forceinline__ bf16_t f2bf(float f) { return (bf16_t)(cvt_pk_bf16(f, 0.f) & 0xffffu); }
; __device__ __forceinline__ void gmlp_item(const bf16_t* __restrict__ proj, const epi::ss_t* __restrict__ ssv, const float* __restrict__ vgain, const bf16_t* __restrict__ wsb_l, const float* __restrict__ bs_l, ...
;     ...
; #pragma unroll
;     for (int ks = 0; ks < 8; ++ks) { const bf16x8 af = *(const bf16x8*)(wsb_l + ((size_t)g * 128 + 32 * qb + r32) * 128 + 16 * ks + 8 * hi);
;         const bf16x8 b0 = *(const LAS bf16x8*)(lds + ((64 * ch + r32) * 136 + 16 * ks + 8 * hi) * 2), b1 = *(const LAS bf16x8*)(lds + ((64 * ch + 32 + r32) * 136 + 16 * ks + 8 * hi) * 2);
;         a0 = __builtin_amdgcn_mfma_f32_32x32x16_bf16(af, b0, a0, 0, 0, 0); a1 = __builtin_amdgcn_mfma_f32_32x32x16_bf16(af, b1, a1, 0, 0, 0); }
; #pragma unroll
;     for (int r = 0; r < 16; ++r) { const int q = 32 * qb + (r & 3) + 8 * (r >> 2) + 4 * hi, tok = tok0 + q; const float bq = bs_l[g * 128 + q];
;         const int c0 = g * 128 + 64 * ch + r32;
;         mlpo[(size_t)tok * 1024 + c0] = f2bf(bf2f(proj[(size_t)tok * NIN + C_ZU + c0]) * (a0[r] + bq));
;         mlpo[(size_t)tok * 1024 + c0 + 32] = f2bf(bf2f(proj[(size_t)tok * NIN + C_ZU + c0 + 32]) * (a1[r] + bq)); }
	global_load_dwordx4 v[2:5], v[44:45], off
	global_load_dwordx4 v[100:103], v[44:45], off offset:32
	ds_read_b128 v[6:9], v98
	ds_read_b128 v[104:107], v98 offset:32
	s_waitcnt vmcnt(1) lgkmcnt(1)
	v_mfma_f32_32x32x16_bf16 v[18:33], v[2:5], v[6:9], 0
	ds_read_b128 v[6:9], v98 offset:8704
	ds_read_b128 v[108:111], v98 offset:8736
	s_waitcnt vmcnt(0) lgkmcnt(2)
	v_mfma_f32_32x32x16_bf16 v[18:33], v[100:103], v[104:107], v[18:33]
	global_load_dwordx4 v[104:107], v[44:45], off offset:64
	s_waitcnt lgkmcnt(1)
	v_mfma_f32_32x32x16_bf16 v[2:17], v[2:5], v[6:9], 0
	s_waitcnt lgkmcnt(0)
	v_mfma_f32_32x32x16_bf16 v[2:17], v[100:103], v[108:111], v[2:17]
	global_load_dwordx4 v[100:103], v[44:45], off offset:96
	ds_read_b128 v[108:111], v98 offset:64
	ds_read_b128 v[112:115], v98 offset:96
	s_waitcnt vmcnt(1) lgkmcnt(1)
	v_mfma_f32_32x32x16_bf16 v[18:33], v[104:107], v[108:111], v[18:33]
	ds_read_b128 v[108:111], v98 offset:8768
	ds_read_b128 v[116:119], v98 offset:8800
	s_waitcnt lgkmcnt(1)
	v_mfma_f32_32x32x16_bf16 v[2:17], v[104:107], v[108:111], v[2:17]
	global_load_dwordx4 v[104:107], v[44:45], off offset:128
	s_waitcnt vmcnt(1)
	v_mfma_f32_32x32x16_bf16 v[18:33], v[100:103], v[112:115], v[18:33]
	s_waitcnt lgkmcnt(0)
	v_mfma_f32_32x32x16_bf16 v[2:17], v[100:103], v[116:119], v[2:17]
	global_load_dwordx4 v[100:103], v[44:45], off offset:160
	ds_read_b128 v[108:111], v98 offset:128
	ds_read_b128 v[112:115], v98 offset:160
	s_waitcnt vmcnt(1) lgkmcnt(1)
	v_mfma_f32_32x32x16_bf16 v[18:33], v[104:107], v[108:111], v[18:33]
	ds_read_b128 v[108:111], v98 offset:8832
	ds_read_b128 v[116:119], v98 offset:8864
	s_waitcnt lgkmcnt(1)
	v_mfma_f32_32x32x16_bf16 v[2:17], v[104:107], v[108:111], v[2:17]
	global_load_dwordx4 v[104:107], v[44:45], off offset:192
	global_load_dwordx4 v[108:111], v[44:45], off offset:224
	s_nop 0
	s_waitcnt vmcnt(2)
	v_mfma_f32_32x32x16_bf16 v[18:33], v[100:103], v[112:115], v[18:33]
	s_waitcnt vmcnt(0)
	s_waitcnt lgkmcnt(0)
	v_mfma_f32_32x32x16_bf16 v[2:17], v[100:103], v[116:119], v[2:17]
	ds_read_b128 v[100:103], v98 offset:192
	ds_read_b128 v[112:115], v98 offset:224
	s_waitcnt lgkmcnt(1)
	v_mfma_f32_32x32x16_bf16 v[18:33], v[104:107], v[100:103], v[18:33]
	ds_read_b128 v[100:103], v98 offset:8896
	ds_read_b128 v[116:119], v98 offset:8928
	s_waitcnt lgkmcnt(2)
	v_mfma_f32_32x32x16_bf16 v[18:33], v[108:111], v[112:115], v[18:33]
	s_waitcnt lgkmcnt(1)
	v_mfma_f32_32x32x16_bf16 v[2:17], v[104:107], v[100:103], v[2:17]
	s_waitcnt lgkmcnt(0)
	v_mfma_f32_32x32x16_bf16 v[2:17], v[108:111], v[116:119], v[2:17]
	s_mov_b32 s101, 0
	v_mad_i64_i32 v[100:101], s[20:21], v120, s14, v[40:41]
	v_and_b32_e32 v248, 3, v0
	v_mov_b32_e32 v251, 0
	v_mul_u32_u24_e32 v250, 0x53fe, v248
	v_lshl_add_u64 v[100:101], v[100:101], 0, v[42:43]
	v_ashrrev_i32_e32 v121, 31, v120
	v_lshl_add_u64 v[100:101], v[250:251], 0, v[100:101]
	v_lshlrev_b64 v[102:103], 11, v[120:121]
	v_lshl_add_u64 v[100:101], v[100:101], 0, s[8:9]
	v_lshl_add_u64 v[44:45], s[26:27], 0, v[42:43]
	v_mul_u32_u24_e32 v250, 0x7fe, v248
	v_lshl_add_u64 v[102:103], v[44:45], 0, v[102:103]
	v_lshl_add_u32 v249, v248, 2, v99
	v_lshl_add_u64 v[102:103], v[250:251], 0, v[102:103]
	global_load_dwordx2 v[104:105], v[100:101], off
	global_load_dwordx2 v[106:107], v[100:101], off offset:64
	global_load_dword v252, v249, s[18:19]
	s_mov_b32 s100, 0x2a000
	v_lshl_add_u64 v[122:123], v[100:101], 0, s[100:101]
	global_load_dwordx2 v[108:109], v[122:123], off
	global_load_dwordx2 v[110:111], v[122:123], off offset:64
	global_load_dword v253, v249, s[18:19] offset:32
	s_mov_b32 s100, 0x54000
	v_lshl_add_u64 v[122:123], v[100:101], 0, s[100:101]
	global_load_dwordx2 v[112:113], v[122:123], off
	global_load_dwordx2 v[114:115], v[122:123], off offset:64
	global_load_dword v254, v249, s[18:19] offset:64
	s_mov_b32 s100, 0x7e000
	v_lshl_add_u64 v[122:123], v[100:101], 0, s[100:101]
	global_load_dwordx2 v[116:117], v[122:123], off
	global_load_dwordx2 v[118:119], v[122:123], off offset:64
	global_load_dword v255, v249, s[18:19] offset:96
	s_mov_b32 vcc_lo, 0xaaaaaaaa
	s_mov_b32 vcc_hi, 0xaaaaaaaa
	s_nop 1
	v_mov_b32_e32 v121, v19
	v_mov_b32_e32 v124, v21
	v_mov_b32_e32 v125, v3
	v_mov_b32_e32 v44, v5
	v_cndmask_b32_dpp v19, v18, v19, vcc quad_perm:[1,0,3,2] row_mask:0xf bank_mask:0xf
	v_cndmask_b32_dpp v21, v20, v21, vcc quad_perm:[1,0,3,2] row_mask:0xf bank_mask:0xf
	v_cndmask_b32_dpp v3, v2, v3, vcc quad_perm:[1,0,3,2] row_mask:0xf bank_mask:0xf
	v_cndmask_b32_dpp v5, v4, v5, vcc quad_perm:[1,0,3,2] row_mask:0xf bank_mask:0xf
	s_mov_b32 vcc_lo, 0x55555555
	s_mov_b32 vcc_hi, 0x55555555
	s_nop 1
	v_cndmask_b32_dpp v18, v121, v18, vcc quad_perm:[1,0,3,2] row_mask:0xf bank_mask:0xf
	v_cndmask_b32_dpp v20, v124, v20, vcc quad_perm:[1,0,3,2] row_mask:0xf bank_mask:0xf
	v_cndmask_b32_dpp v2, v125, v2, vcc quad_perm:[1,0,3,2] row_mask:0xf bank_mask:0xf
	v_cndmask_b32_dpp v4, v44, v4, vcc quad_perm:[1,0,3,2] row_mask:0xf bank_mask:0xf
	s_mov_b32 vcc_lo, 0xcccccccc
	s_mov_b32 vcc_hi, 0xcccccccc
	s_nop 1
	v_mov_b32_e32 v121, v20
	v_mov_b32_e32 v124, v21
	v_mov_b32_e32 v125, v4
	v_mov_b32_e32 v44, v5
	v_cndmask_b32_dpp v20, v18, v20, vcc quad_perm:[2,3,0,1] row_mask:0xf bank_mask:0xf
	v_cndmask_b32_dpp v21, v19, v21, vcc quad_perm:[2,3,0,1] row_mask:0xf bank_mask:0xf
	v_cndmask_b32_dpp v4, v2, v4, vcc quad_perm:[2,3,0,1] row_mask:0xf bank_mask:0xf
	v_cndmask_b32_dpp v5, v3, v5, vcc quad_perm:[2,3,0,1] row_mask:0xf bank_mask:0xf
	s_mov_b32 vcc_lo, 0x33333333
	s_mov_b32 vcc_hi, 0x33333333
	s_nop 1
	v_cndmask_b32_dpp v18, v121, v18, vcc quad_perm:[2,3,0,1] row_mask:0xf bank_mask:0xf
; __device__ __forceinline__ float bf2f(bf16_t b) { return __uint_as_float((unsigned)b << 16); }
; __device__ __forceinline__ bf16_t f2bf(float f) { return (bf16_t)(cvt_pk_bf16(f, 0.f) & 0xffffu); }
; __device__ __forceinline__ void gmlp_item(const bf16_t* __restrict__ proj, const epi::ss_t* __restrict__ ssv, const float* __restrict__ vgain, const bf16_t* __restrict__ wsb_l, const float* __restrict__ bs_l, ...
;     ...
;     for (int r = 0; r < 16; ++r) { const int q = 32 * qb + (r & 3) + 8 * (r >> 2) + 4 * hi, tok = tok0 + q; const float bq = bs_l[g * 128 + q];
;         const int c0 = g * 128 + 64 * ch + r32;
;         mlpo[(size_t)tok * 1024 + c0] = f2bf(bf2f(proj[(size_t)tok * NIN + C_ZU + c0]) * (a0[r] + bq));
;         mlpo[(size_t)tok * 1024 + c0 + 32] = f2bf(bf2f(proj[(size_t)tok * NIN + C_ZU + c0 + 32]) * (a1[r] + bq)); }
	v_cndmask_b32_dpp v19, v124, v19, vcc quad_perm:[2,3,0,1] row_mask:0xf bank_mask:0xf
	v_cndmask_b32_dpp v2, v125, v2, vcc quad_perm:[2,3,0,1] row_mask:0xf bank_mask:0xf
	v_cndmask_b32_dpp v3, v44, v3, vcc quad_perm:[2,3,0,1] row_mask:0xf bank_mask:0xf
	s_mov_b32 vcc_lo, 0xaaaaaaaa
	s_mov_b32 vcc_hi, 0xaaaaaaaa
	s_nop 1
	v_mov_b32_e32 v121, v23
	v_mov_b32_e32 v124, v25
	v_mov_b32_e32 v125, v7
	v_mov_b32_e32 v44, v9
	v_cndmask_b32_dpp v23, v22, v23, vcc quad_perm:[1,0,3,2] row_mask:0xf bank_mask:0xf
	v_cndmask_b32_dpp v25, v24, v25, vcc quad_perm:[1,0,3,2] row_mask:0xf bank_mask:0xf
	v_cndmask_b32_dpp v7, v6, v7, vcc quad_perm:[1,0,3,2] row_mask:0xf bank_mask:0xf
	v_cndmask_b32_dpp v9, v8, v9, vcc quad_perm:[1,0,3,2] row_mask:0xf bank_mask:0xf
	s_mov_b32 vcc_lo, 0x55555555
	s_mov_b32 vcc_hi, 0x55555555
	s_nop 1
	v_cndmask_b32_dpp v22, v121, v22, vcc quad_perm:[1,0,3,2] row_mask:0xf bank_mask:0xf
	v_cndmask_b32_dpp v24, v124, v24, vcc quad_perm:[1,0,3,2] row_mask:0xf bank_mask:0xf
	v_cndmask_b32_dpp v6, v125, v6, vcc quad_perm:[1,0,3,2] row_mask:0xf bank_mask:0xf
	v_cndmask_b32_dpp v8, v44, v8, vcc quad_perm:[1,0,3,2] row_mask:0xf bank_mask:0xf
	s_mov_b32 vcc_lo, 0xcccccccc
	s_mov_b32 vcc_hi, 0xcccccccc
	s_nop 1
	v_mov_b32_e32 v121, v24
	v_mov_b32_e32 v124, v25
	v_mov_b32_e32 v125, v8
	v_mov_b32_e32 v44, v9
	v_cndmask_b32_dpp v24, v22, v24, vcc quad_perm:[2,3,0,1] row_mask:0xf bank_mask:0xf
	v_cndmask_b32_dpp v25, v23, v25, vcc quad_perm:[2,3,0,1] row_mask:0xf bank_mask:0xf
	v_cndmask_b32_dpp v8, v6, v8, vcc quad_perm:[2,3,0,1] row_mask:0xf bank_mask:0xf
	v_cndmask_b32_dpp v9, v7, v9, vcc quad_perm:[2,3,0,1] row_mask:0xf bank_mask:0xf
	s_mov_b32 vcc_lo, 0x33333333
	s_mov_b32 vcc_hi, 0x33333333
	s_nop 1
	v_cndmask_b32_dpp v22, v121, v22, vcc quad_perm:[2,3,0,1] row_mask:0xf bank_mask:0xf
	v_cndmask_b32_dpp v23, v124, v23, vcc quad_perm:[2,3,0,1] row_mask:0xf bank_mask:0xf
	v_cndmask_b32_dpp v6, v125, v6, vcc quad_perm:[2,3,0,1] row_mask:0xf bank_mask:0xf
	v_cndmask_b32_dpp v7, v44, v7, vcc quad_perm:[2,3,0,1] row_mask:0xf bank_mask:0xf
	s_mov_b32 vcc_lo, 0xaaaaaaaa
	s_mov_b32 vcc_hi, 0xaaaaaaaa
	s_nop 1
	v_mov_b32_e32 v121, v27
	v_mov_b32_e32 v124, v29
	v_mov_b32_e32 v125, v11
	v_mov_b32_e32 v44, v13
	v_cndmask_b32_dpp v27, v26, v27, vcc quad_perm:[1,0,3,2] row_mask:0xf bank_mask:0xf
	v_cndmask_b32_dpp v29, v28, v29, vcc quad_perm:[1,0,3,2] row_mask:0xf bank_mask:0xf
	v_cndmask_b32_dpp v11, v10, v11, vcc quad_perm:[1,0,3,2] row_mask:0xf bank_mask:0xf
	v_cndmask_b32_dpp v13, v12, v13, vcc quad_perm:[1,0,3,2] row_mask:0xf bank_mask:0xf
	s_mov_b32 vcc_lo, 0x55555555
	s_mov_b32 vcc_hi, 0x55555555
	s_nop 1
	v_cndmask_b32_dpp v26, v121, v26, vcc quad_perm:[1,0,3,2] row_mask:0xf bank_mask:0xf
	v_cndmask_b32_dpp v28, v124, v28, vcc quad_perm:[1,0,3,2] row_mask:0xf bank_mask:0xf
	v_cndmask_b32_dpp v10, v125, v10, vcc quad_perm:[1,0,3,2] row_mask:0xf bank_mask:0xf
	v_cndmask_b32_dpp v12, v44, v12, vcc quad_perm:[1,0,3,2] row_mask:0xf bank_mask:0xf
	s_mov_b32 vcc_lo, 0xcccccccc
	s_mov_b32 vcc_hi, 0xcccccccc
	s_nop 1
	v_mov_b32_e32 v121, v28
	v_mov_b32_e32 v124, v29
	v_mov_b32_e32 v125, v12
	v_mov_b32_e32 v44, v13
	v_cndmask_b32_dpp v28, v26, v28, vcc quad_perm:[2,3,0,1] row_mask:0xf bank_mask:0xf
	v_cndmask_b32_dpp v29, v27, v29, vcc quad_perm:[2,3,0,1] row_mask:0xf bank_mask:0xf
	v_cndmask_b32_dpp v12, v10, v12, vcc quad_perm:[2,3,0,1] row_mask:0xf bank_mask:0xf
	v_cndmask_b32_dpp v13, v11, v13, vcc quad_perm:[2,3,0,1] row_mask:0xf bank_mask:0xf
	s_mov_b32 vcc_lo, 0x33333333
	s_mov_b32 vcc_hi, 0x33333333
	s_nop 1
	v_cndmask_b32_dpp v26, v121, v26, vcc quad_perm:[2,3,0,1] row_mask:0xf bank_mask:0xf
	v_cndmask_b32_dpp v27, v124, v27, vcc quad_perm:[2,3,0,1] row_mask:0xf bank_mask:0xf
	v_cndmask_b32_dpp v10, v125, v10, vcc quad_perm:[2,3,0,1] row_mask:0xf bank_mask:0xf
	v_cndmask_b32_dpp v11, v44, v11, vcc quad_perm:[2,3,0,1] row_mask:0xf bank_mask:0xf
	s_mov_b32 vcc_lo, 0xaaaaaaaa
	s_mov_b32 vcc_hi, 0xaaaaaaaa
	s_nop 1
	v_mov_b32_e32 v121, v31
	v_mov_b32_e32 v124, v33
	v_mov_b32_e32 v125, v15
	v_mov_b32_e32 v44, v17
	v_cndmask_b32_dpp v31, v30, v31, vcc quad_perm:[1,0,3,2] row_mask:0xf bank_mask:0xf
	v_cndmask_b32_dpp v33, v32, v33, vcc quad_perm:[1,0,3,2] row_mask:0xf bank_mask:0xf
	v_cndmask_b32_dpp v15, v14, v15, vcc quad_perm:[1,0,3,2] row_mask:0xf bank_mask:0xf
	v_cndmask_b32_dpp v17, v16, v17, vcc quad_perm:[1,0,3,2] row_mask:0xf bank_mask:0xf
	s_mov_b32 vcc_lo, 0x55555555
	s_mov_b32 vcc_hi, 0x55555555
	s_nop 1
	v_cndmask_b32_dpp v30, v121, v30, vcc quad_perm:[1,0,3,2] row_mask:0xf bank_mask:0xf
	v_cndmask_b32_dpp v32, v124, v32, vcc quad_perm:[1,0,3,2] row_mask:0xf bank_mask:0xf
	v_cndmask_b32_dpp v14, v125, v14, vcc quad_perm:[1,0,3,2] row_mask:0xf bank_mask:0xf
	v_cndmask_b32_dpp v16, v44, v16, vcc quad_perm:[1,0,3,2] row_mask:0xf bank_mask:0xf
	s_mov_b32 vcc_lo, 0xcccccccc
	s_mov_b32 vcc_hi, 0xcccccccc
	s_nop 1
	v_mov_b32_e32 v121, v32
	v_mov_b32_e32 v124, v33
	v_mov_b32_e32 v125, v16
	v_mov_b32_e32 v44, v17
	v_cndmask_b32_dpp v32, v30, v32, vcc quad_perm:[2,3,0,1] row_mask:0xf bank_mask:0xf
	v_cndmask_b32_dpp v33, v31, v33, vcc quad_perm:[2,3,0,1] row_mask:0xf bank_mask:0xf
	v_cndmask_b32_dpp v16, v14, v16, vcc quad_perm:[2,3,0,1] row_mask:0xf bank_mask:0xf
	v_cndmask_b32_dpp v17, v15, v17, vcc quad_perm:[2,3,0,1] row_mask:0xf bank_mask:0xf
	s_mov_b32 vcc_lo, 0x33333333
	s_mov_b32 vcc_hi, 0x33333333
	s_nop 1
	v_cndmask_b32_dpp v30, v121, v30, vcc quad_perm:[2,3,0,1] row_mask:0xf bank_mask:0xf
	v_cndmask_b32_dpp v31, v124, v31, vcc quad_perm:[2,3,0,1] row_mask:0xf bank_mask:0xf
	v_cndmask_b32_dpp v14, v125, v14, vcc quad_perm:[2,3,0,1] row_mask:0xf bank_mask:0xf
	v_cndmask_b32_dpp v15, v44, v15, vcc quad_perm:[2,3,0,1] row_mask:0xf bank_mask:0xf
	s_waitcnt vmcnt(0)
; __device__ __forceinline__ float bf2f(bf16_t b) { return __uint_as_float((unsigned)b << 16); }
; __device__ __forceinline__ bf16_t f2bf(float f) { return (bf16_t)(cvt_pk_bf16(f, 0.f) & 0xffffu); }
; __device__ __forceinline__ void gmlp_item(const bf16_t* __restrict__ proj, const epi::ss_t* __restrict__ ssv, const float* __restrict__ vgain, const bf16_t* __restrict__ wsb_l, const float* __restrict__ bs_l, ...
;     ...
;     for (int r = 0; r < 16; ++r) { const int q = 32 * qb + (r & 3) + 8 * (r >> 2) + 4 * hi, tok = tok0 + q; const float bq = bs_l[g * 128 + q];
;         const int c0 = g * 128 + 64 * ch + r32;
;         mlpo[(size_t)tok * 1024 + c0] = f2bf(bf2f(proj[(size_t)tok * NIN + C_ZU + c0]) * (a0[r] + bq));
;         mlpo[(size_t)tok * 1024 + c0 + 32] = f2bf(bf2f(proj[(size_t)tok * NIN + C_ZU + c0 + 32]) * (a1[r] + bq)); }
;     __syncthreads();
	v_lshlrev_b32_e32 v121, 16, v104
	v_and_b32_e32 v124, 0xffff0000, v104
	v_lshlrev_b32_e32 v125, 16, v105
	v_and_b32_e32 v44, 0xffff0000, v105
	v_add_f32_e32 v18, v18, v252
	v_add_f32_e32 v19, v19, v252
	v_add_f32_e32 v20, v20, v252
	v_add_f32_e32 v21, v21, v252
	v_mul_f32_e32 v18, v18, v121
	v_mul_f32_e32 v19, v19, v124
	v_mul_f32_e32 v20, v20, v125
	v_mul_f32_e32 v21, v21, v44
	v_cvt_pk_bf16_f32 v18, v18, v19
	v_cvt_pk_bf16_f32 v19, v20, v21
	global_store_dwordx2 v[102:103], v[18:19], off
	v_lshlrev_b32_e32 v121, 16, v106
	v_and_b32_e32 v124, 0xffff0000, v106
	v_lshlrev_b32_e32 v125, 16, v107
	v_and_b32_e32 v44, 0xffff0000, v107
	v_add_f32_e32 v2, v2, v252
	v_add_f32_e32 v3, v3, v252
	v_add_f32_e32 v4, v4, v252
	v_add_f32_e32 v5, v5, v252
	v_mul_f32_e32 v2, v2, v121
	v_mul_f32_e32 v3, v3, v124
	v_mul_f32_e32 v4, v4, v125
	v_mul_f32_e32 v5, v5, v44
	v_cvt_pk_bf16_f32 v2, v2, v3
	v_cvt_pk_bf16_f32 v3, v4, v5
	global_store_dwordx2 v[102:103], v[2:3], off offset:64
	s_mov_b32 s100, 0x4000
	v_lshl_add_u64 v[122:123], v[102:103], 0, s[100:101]
	v_lshlrev_b32_e32 v121, 16, v108
	v_and_b32_e32 v124, 0xffff0000, v108
	v_lshlrev_b32_e32 v125, 16, v109
	v_and_b32_e32 v44, 0xffff0000, v109
	v_add_f32_e32 v22, v22, v253
	v_add_f32_e32 v23, v23, v253
	v_add_f32_e32 v24, v24, v253
	v_add_f32_e32 v25, v25, v253
	v_mul_f32_e32 v22, v22, v121
	v_mul_f32_e32 v23, v23, v124
	v_mul_f32_e32 v24, v24, v125
	v_mul_f32_e32 v25, v25, v44
	v_cvt_pk_bf16_f32 v22, v22, v23
	v_cvt_pk_bf16_f32 v23, v24, v25
	global_store_dwordx2 v[122:123], v[22:23], off
	v_lshlrev_b32_e32 v121, 16, v110
	v_and_b32_e32 v124, 0xffff0000, v110
	v_lshlrev_b32_e32 v125, 16, v111
	v_and_b32_e32 v44, 0xffff0000, v111
	v_add_f32_e32 v6, v6, v253
	v_add_f32_e32 v7, v7, v253
	v_add_f32_e32 v8, v8, v253
	v_add_f32_e32 v9, v9, v253
	v_mul_f32_e32 v6, v6, v121
	v_mul_f32_e32 v7, v7, v124
	v_mul_f32_e32 v8, v8, v125
	v_mul_f32_e32 v9, v9, v44
	v_cvt_pk_bf16_f32 v6, v6, v7
	v_cvt_pk_bf16_f32 v7, v8, v9
	global_store_dwordx2 v[122:123], v[6:7], off offset:64
	s_mov_b32 s100, 0x8000
	v_lshl_add_u64 v[122:123], v[102:103], 0, s[100:101]
	v_lshlrev_b32_e32 v121, 16, v112
	v_and_b32_e32 v124, 0xffff0000, v112
	v_lshlrev_b32_e32 v125, 16, v113
	v_and_b32_e32 v44, 0xffff0000, v113
	v_add_f32_e32 v26, v26, v254
	v_add_f32_e32 v27, v27, v254
	v_add_f32_e32 v28, v28, v254
	v_add_f32_e32 v29, v29, v254
	v_mul_f32_e32 v26, v26, v121
	v_mul_f32_e32 v27, v27, v124
	v_mul_f32_e32 v28, v28, v125
	v_mul_f32_e32 v29, v29, v44
	v_cvt_pk_bf16_f32 v26, v26, v27
	v_cvt_pk_bf16_f32 v27, v28, v29
	global_store_dwordx2 v[122:123], v[26:27], off
	v_lshlrev_b32_e32 v121, 16, v114
	v_and_b32_e32 v124, 0xffff0000, v114
	v_lshlrev_b32_e32 v125, 16, v115
	v_and_b32_e32 v44, 0xffff0000, v115
	v_add_f32_e32 v10, v10, v254
	v_add_f32_e32 v11, v11, v254
	v_add_f32_e32 v12, v12, v254
	v_add_f32_e32 v13, v13, v254
	v_mul_f32_e32 v10, v10, v121
	v_mul_f32_e32 v11, v11, v124
	v_mul_f32_e32 v12, v12, v125
	v_mul_f32_e32 v13, v13, v44
	v_cvt_pk_bf16_f32 v10, v10, v11
	v_cvt_pk_bf16_f32 v11, v12, v13
	global_store_dwordx2 v[122:123], v[10:11], off offset:64
	s_mov_b32 s100, 0xc000
	v_lshl_add_u64 v[122:123], v[102:103], 0, s[100:101]
	v_lshlrev_b32_e32 v121, 16, v116
	v_and_b32_e32 v124, 0xffff0000, v116
	v_lshlrev_b32_e32 v125, 16, v117
	v_and_b32_e32 v44, 0xffff0000, v117
	v_add_f32_e32 v30, v30, v255
	v_add_f32_e32 v31, v31, v255
	v_add_f32_e32 v32, v32, v255
	v_add_f32_e32 v33, v33, v255
	v_mul_f32_e32 v30, v30, v121
	v_mul_f32_e32 v31, v31, v124
	v_mul_f32_e32 v32, v32, v125
	v_mul_f32_e32 v33, v33, v44
	v_cvt_pk_bf16_f32 v30, v30, v31
	v_cvt_pk_bf16_f32 v31, v32, v33
	global_store_dwordx2 v[122:123], v[30:31], off
	v_lshlrev_b32_e32 v121, 16, v118
	v_and_b32_e32 v124, 0xffff0000, v118
	v_lshlrev_b32_e32 v125, 16, v119
	v_and_b32_e32 v44, 0xffff0000, v119
	v_add_f32_e32 v14, v14, v255
	v_add_f32_e32 v15, v15, v255
	v_add_f32_e32 v16, v16, v255
	v_add_f32_e32 v17, v17, v255
	v_mul_f32_e32 v14, v14, v121
	v_mul_f32_e32 v15, v15, v124
	v_mul_f32_e32 v16, v16, v125
	v_mul_f32_e32 v17, v17, v44
	v_cvt_pk_bf16_f32 v14, v14, v15
	v_cvt_pk_bf16_f32 v15, v16, v17
	global_store_dwordx2 v[122:123], v[14:15], off offset:64
	s_barrier
	s_cbranch_scc1 .LBB0_651

; #define LAS __attribute__((address_space(3)))
; __device__ __forceinline__ bf16_t f2bf(float f) { return (bf16_t)(cvt_pk_bf16(f, 0.f) & 0xffffu); }
; __device__ __forceinline__ void unpack8(u32x4 w, f32x4& v0, f32x4& v1) { v0 = (f32x4){bf_lo(w.x), bf_hi(w.x), bf_lo(w.y), bf_hi(w.y)}; v1 = (f32x4){bf_lo(w.z), bf_hi(w.z), bf_lo(w.w), bf_hi(w.w)}; }
; __device__ __forceinline__ float ss_val(const ss_t* ss, int row) { return (float)ss[row] * (1.f / 16777216.f); }
; __device__ __forceinline__ void gmlp_item(const bf16_t* __restrict__ proj, const epi::ss_t* __restrict__ ssv, const float* __restrict__ vgain, const bf16_t* __restrict__ wsb_l, const float* __restrict__ bs_l, ...
;     ...
;     { const int p = tid >> 2, cb = (tid & 3) * 32; const float rs = rsqrtf(epi::ss_val(ssv, tok0 + p) * (1.f / 1024.f) + EPS);
; #pragma unroll
;       for (int cc = 0; cc < 4; ++cc) { const int c0 = cb + cc * 8; f32x4 v0, v1; epi::unpack8(*(const u32x4*)(proj + (size_t)(tok0 + p) * NIN + C_ZV + g * 128 + c0), v0, v1);
;           const f32x4 g0 = *(const f32x4*)(vgain + g * 128 + c0), g1 = *(const f32x4*)(vgain + g * 128 + c0 + 4);
; #pragma unroll
;           for (int i = 0; i < 4; ++i) { *(LAS bf16_t*)(lds + ((c0 + i) * 136 + p) * 2) = f2bf(v0[i] * rs * g0[i]); *(LAS bf16_t*)(lds + ((c0 + 4 + i) * 136 + p) * 2) = f2bf(v1[i] * rs * g1[i]); } } }
;     __syncthreads();
.LBB0_1629:
	s_and_b32 s19, s3, 0xffffff80
	v_or_b32_e32 v4, s19, v46
	v_mov_b64_e32 v[40:41], s[34:35]
	v_ashrrev_i32_e32 v5, 31, v4
	v_mad_i64_i32 v[6:7], s[22:23], v4, s16, v[40:41]
	v_lshl_add_u64 v[4:5], v[4:5], 3, s[68:69]
	global_load_dwordx2 v[14:15], v[4:5], off
	s_and_b32 s20, s13, 0x380
	s_lshl_b32 s4, s20, 1
	v_or_b32_e32 v2, s20, v47
	v_mov_b32_e32 v3, v35
	v_lshlrev_b32_e32 v2, 8, v2
	v_lshl_add_u64 v[6:7], v[6:7], 0, s[4:5]
	v_lshl_add_u64 v[44:45], v[36:37], 0, v[2:3]
	v_lshl_add_u64 v[2:3], v[6:7], 0, v[34:35]
	s_lshl_b32 s4, s20, 2
	v_add_co_u32_e32 v10, vcc, s17, v2
	v_lshl_add_u64 v[16:17], v[38:39], 0, s[4:5]
	s_nop 0
	v_addc_co_u32_e32 v11, vcc, 0, v3, vcc
	v_lshl_add_u64 v[18:19], v[2:3], 0, s[8:9]
	global_load_dwordx4 v[2:5], v[16:17], off offset:16
	global_load_dwordx4 v[6:9], v[16:17], off
	s_nop 0
	global_load_dwordx4 v[10:13], v[10:11], off offset:3072
	v_or_b32_e32 v42, s20, v48
	v_or_b32_e32 v128, s19, v49
	v_mov_b32_e32 v43, v35
	v_lshlrev_b32_e32 v42, 1, v42
	v_or_b32_e32 v99, s20, v49
	v_lshlrev_b32_e32 v99, 2, v99
	s_add_i32 s18, s18, s33
	s_add_i32 s3, s3, s12
	s_add_i32 s13, s13, s14
	s_cmpk_lt_i32 s18, 0x200
	s_waitcnt vmcnt(3)
	v_ffbh_u32_e32 v20, v15
	v_min_u32_e32 v20, 32, v20
	v_lshlrev_b64 v[14:15], v20, v[14:15]
	v_min_u32_e32 v14, 1, v14
	v_or_b32_e32 v14, v15, v14
	v_cvt_f32_u32_e32 v14, v14
	v_sub_u32_e32 v20, 32, v20
	v_ldexp_f32 v14, v14, v20
	v_mul_f32_e32 v14, 0x33800000, v14
	v_fmamk_f32 v14, v14, 0x3a800000, v65
	v_mul_f32_e32 v15, 0x4b800000, v14
	v_cmp_gt_f32_e32 vcc, s15, v14
	s_waitcnt vmcnt(0)
	v_lshlrev_b32_e32 v21, 16, v10
	v_cndmask_b32_e32 v14, v14, v15, vcc
	v_rsq_f32_e32 v14, v14
	v_lshlrev_b32_e32 v23, 16, v12
	v_and_b32_e32 v10, 0xffff0000, v10
	v_and_b32_e32 v12, 0xffff0000, v12
	v_mul_f32_e32 v15, 0x45800000, v14
	v_cndmask_b32_e32 v14, v14, v15, vcc
	v_mul_f32_e32 v15, v14, v21
	v_mul_f32_e32 v20, v14, v23
	v_mul_f32_e32 v6, v6, v15
	v_mul_f32_e32 v2, v2, v20
	v_mul_f32_e32 v10, v14, v10
	v_cvt_pk_bf16_f32 v6, v6, v35
	ds_write_b16 v66, v6
	v_cvt_pk_bf16_f32 v2, v2, v35
	v_lshlrev_b32_e32 v22, 16, v11
	v_mul_f32_e32 v12, v14, v12
	v_mul_f32_e32 v7, v7, v10
	ds_write_b16 v67, v2
	v_cvt_pk_bf16_f32 v2, v7, v35
	v_lshlrev_b32_e32 v24, 16, v13
	v_mul_f32_e32 v21, v14, v22
	v_mul_f32_e32 v3, v3, v12
	ds_write_b16 v68, v2
	v_cvt_pk_bf16_f32 v2, v3, v35
	v_and_b32_e32 v11, 0xffff0000, v11
	v_and_b32_e32 v13, 0xffff0000, v13
	v_mul_f32_e32 v22, v14, v24
	v_mul_f32_e32 v8, v8, v21
	ds_write_b16 v69, v2
	v_cvt_pk_bf16_f32 v2, v8, v35
	v_mul_f32_e32 v11, v14, v11
	v_mul_f32_e32 v13, v14, v13
	v_mul_f32_e32 v4, v4, v22
	ds_write_b16 v70, v2
	v_cvt_pk_bf16_f32 v2, v4, v35
	v_mul_f32_e32 v9, v9, v11
	v_mul_f32_e32 v5, v5, v13
	ds_write_b16 v71, v2
	v_cvt_pk_bf16_f32 v2, v9, v35
	ds_write_b16 v72, v2
	v_cvt_pk_bf16_f32 v15, v5, v35
	global_load_dwordx4 v[2:5], v[18:19], off offset:16
	global_load_dwordx4 v[6:9], v[16:17], off offset:32
	global_load_dwordx4 v[10:13], v[16:17], off offset:48
	ds_write_b16 v73, v15
	s_waitcnt vmcnt(2)
	v_lshlrev_b32_e32 v15, 16, v2
	v_and_b32_e32 v2, 0xffff0000, v2
	v_mul_f32_e32 v15, v14, v15
	v_lshlrev_b32_e32 v21, 16, v4
	v_mul_f32_e32 v2, v14, v2
	s_waitcnt vmcnt(1)
	v_mul_f32_e32 v6, v6, v15
	v_and_b32_e32 v4, 0xffff0000, v4
	v_mul_f32_e32 v21, v14, v21
	v_mul_f32_e32 v2, v7, v2
	v_cvt_pk_bf16_f32 v6, v6, v35
	v_lshlrev_b32_e32 v20, 16, v3
	v_mul_f32_e32 v4, v14, v4
	s_waitcnt vmcnt(0)
	v_mul_f32_e32 v10, v10, v21
	ds_write_b16 v74, v6
	v_cvt_pk_bf16_f32 v6, v10, v35
	ds_write_b16 v75, v6
	v_cvt_pk_bf16_f32 v2, v2, v35
	v_lshlrev_b32_e32 v22, 16, v5
	v_mul_f32_e32 v20, v14, v20
	v_mul_f32_e32 v4, v11, v4
	ds_write_b16 v76, v2
	v_cvt_pk_bf16_f32 v2, v4, v35
	v_and_b32_e32 v3, 0xffff0000, v3
	v_and_b32_e32 v5, 0xffff0000, v5
	v_mul_f32_e32 v22, v14, v22
	v_mul_f32_e32 v7, v8, v20
	ds_write_b16 v77, v2
	v_cvt_pk_bf16_f32 v2, v7, v35
	v_mul_f32_e32 v3, v14, v3
	v_mul_f32_e32 v5, v14, v5
	v_mul_f32_e32 v8, v12, v22
	ds_write_b16 v78, v2
	v_cvt_pk_bf16_f32 v2, v8, v35
	v_mul_f32_e32 v3, v9, v3
	v_mul_f32_e32 v5, v13, v5
	ds_write_b16 v79, v2
	v_cvt_pk_bf16_f32 v2, v3, v35
	ds_write_b16 v80, v2
	v_cvt_pk_bf16_f32 v15, v5, v35
	global_load_dwordx4 v[2:5], v[18:19], off offset:32
	global_load_dwordx4 v[6:9], v[16:17], off offset:64
	global_load_dwordx4 v[10:13], v[16:17], off offset:80
	ds_write_b16 v81, v15
	s_waitcnt vmcnt(2)
	v_lshlrev_b32_e32 v15, 16, v2
	v_and_b32_e32 v2, 0xffff0000, v2
	v_mul_f32_e32 v15, v14, v15
	v_lshlrev_b32_e32 v21, 16, v4
	v_mul_f32_e32 v2, v14, v2
	s_waitcnt vmcnt(1)
	v_mul_f32_e32 v6, v6, v15
	v_and_b32_e32 v4, 0xffff0000, v4
	v_mul_f32_e32 v21, v14, v21
	v_mul_f32_e32 v2, v7, v2
	v_cvt_pk_bf16_f32 v6, v6, v35
	v_lshlrev_b32_e32 v20, 16, v3
	v_mul_f32_e32 v4, v14, v4
	s_waitcnt vmcnt(0)
	v_mul_f32_e32 v10, v10, v21
	ds_write_b16 v82, v6
	v_cvt_pk_bf16_f32 v6, v10, v35
	ds_write_b16 v83, v6
	v_cvt_pk_bf16_f32 v2, v2, v35
	v_lshlrev_b32_e32 v22, 16, v5
	v_mul_f32_e32 v20, v14, v20
	v_mul_f32_e32 v4, v11, v4
	ds_write_b16 v84, v2
	v_cvt_pk_bf16_f32 v2, v4, v35
	v_and_b32_e32 v3, 0xffff0000, v3
	v_and_b32_e32 v5, 0xffff0000, v5
	v_mul_f32_e32 v22, v14, v22
	v_mul_f32_e32 v7, v8, v20
	ds_write_b16 v85, v2
	v_cvt_pk_bf16_f32 v2, v7, v35
	v_mul_f32_e32 v3, v14, v3
	v_mul_f32_e32 v5, v14, v5
	v_mul_f32_e32 v8, v12, v22
	ds_write_b16 v86, v2
	v_cvt_pk_bf16_f32 v2, v8, v35
	v_mul_f32_e32 v3, v9, v3
	v_mul_f32_e32 v5, v13, v5
	ds_write_b16 v87, v2
	v_cvt_pk_bf16_f32 v2, v3, v35
	ds_write_b16 v88, v2
	v_cvt_pk_bf16_f32 v15, v5, v35
	global_load_dwordx4 v[2:5], v[18:19], off offset:48
	global_load_dwordx4 v[6:9], v[16:17], off offset:96
	global_load_dwordx4 v[10:13], v[16:17], off offset:112
	ds_write_b16 v89, v15
	s_waitcnt vmcnt(2)
	v_lshlrev_b32_e32 v15, 16, v2
	v_and_b32_e32 v2, 0xffff0000, v2
	v_mul_f32_e32 v15, v14, v15
	v_lshlrev_b32_e32 v17, 16, v4
	v_mul_f32_e32 v2, v14, v2
	s_waitcnt vmcnt(1)
	v_mul_f32_e32 v6, v6, v15
	v_and_b32_e32 v4, 0xffff0000, v4
	v_mul_f32_e32 v17, v14, v17
	v_mul_f32_e32 v2, v7, v2
	v_cvt_pk_bf16_f32 v6, v6, v35
	v_lshlrev_b32_e32 v16, 16, v3
	v_mul_f32_e32 v4, v14, v4
	s_waitcnt vmcnt(0)
	v_mul_f32_e32 v10, v10, v17
	ds_write_b16 v90, v6
	v_cvt_pk_bf16_f32 v6, v10, v35
	ds_write_b16 v91, v6
	v_cvt_pk_bf16_f32 v2, v2, v35
	v_lshlrev_b32_e32 v18, 16, v5
	v_mul_f32_e32 v16, v14, v16
	v_mul_f32_e32 v4, v11, v4
	ds_write_b16 v92, v2
	v_cvt_pk_bf16_f32 v2, v4, v35
	v_and_b32_e32 v3, 0xffff0000, v3
	v_mul_f32_e32 v18, v14, v18
	v_mul_f32_e32 v7, v8, v16
	ds_write_b16 v93, v2
	v_cvt_pk_bf16_f32 v2, v7, v35
	v_and_b32_e32 v5, 0xffff0000, v5
	v_mul_f32_e32 v3, v14, v3
	v_mul_f32_e32 v8, v12, v18
	ds_write_b16 v94, v2
	v_cvt_pk_bf16_f32 v2, v8, v35
	v_mul_f32_e32 v5, v14, v5
	v_mul_f32_e32 v3, v9, v3
	ds_write_b16 v95, v2
	v_cvt_pk_bf16_f32 v2, v3, v35
	v_mul_f32_e32 v5, v13, v5
	ds_write_b16 v96, v2
	v_cvt_pk_bf16_f32 v2, v5, v35
	ds_write_b16 v97, v2
	s_waitcnt lgkmcnt(0)
	s_barrier
; #define LAS __attribute__((address_space(3)))
; __device__ __forceinline__ float bf2f(bf16_t b) { return __uint_as_float((unsigned)b << 16); }
; __device__ __forceinline__ bf16_t f2bf(float f) { return (bf16_t)(cvt_pk_bf16(f, 0.f) & 0xffffu); }
; __device__ __forceinline__ void gmlp_item(const bf16_t* __restrict__ proj, const epi::ss_t* __restrict__ ssv, const float* __restrict__ vgain, const bf16_t* __restrict__ wsb_l, const float* __restrict__ bs_l, ...
;     ...
; #pragma unroll
;     for (int ks = 0; ks < 8; ++ks) { const bf16x8 af = *(const bf16x8*)(wsb_l + ((size_t)g * 128 + 32 * qb + r32) * 128 + 16 * ks + 8 * hi);
;         const bf16x8 b0 = *(const LAS bf16x8*)(lds + ((64 * ch + r32) * 136 + 16 * ks + 8 * hi) * 2), b1 = *(const LAS bf16x8*)(lds + ((64 * ch + 32 + r32) * 136 + 16 * ks + 8 * hi) * 2);
;         a0 = __builtin_amdgcn_mfma_f32_32x32x16_bf16(af, b0, a0, 0, 0, 0); a1 = __builtin_amdgcn_mfma_f32_32x32x16_bf16(af, b1, a1, 0, 0, 0); }
; #pragma unroll
;     for (int r = 0; r < 16; ++r) { const int q = 32 * qb + (r & 3) + 8 * (r >> 2) + 4 * hi, tok = tok0 + q; const float bq = bs_l[g * 128 + q];
;         const int c0 = g * 128 + 64 * ch + r32;
;         mlpo[(size_t)tok * 1024 + c0] = f2bf(bf2f(proj[(size_t)tok * NIN + C_ZU + c0]) * (a0[r] + bq));
;         mlpo[(size_t)tok * 1024 + c0 + 32] = f2bf(bf2f(proj[(size_t)tok * NIN + C_ZU + c0 + 32]) * (a1[r] + bq)); }
	global_load_dwordx4 v[2:5], v[44:45], off
	global_load_dwordx4 v[100:103], v[44:45], off offset:32
	ds_read_b128 v[6:9], v98
	ds_read_b128 v[104:107], v98 offset:32
	s_waitcnt vmcnt(1) lgkmcnt(1)
	v_mfma_f32_32x32x16_bf16 v[18:33], v[2:5], v[6:9], 0
	ds_read_b128 v[6:9], v98 offset:8704
	ds_read_b128 v[108:111], v98 offset:8736
	s_waitcnt vmcnt(0) lgkmcnt(2)
	v_mfma_f32_32x32x16_bf16 v[18:33], v[100:103], v[104:107], v[18:33]
	global_load_dwordx4 v[104:107], v[44:45], off offset:64
	s_waitcnt lgkmcnt(1)
	v_mfma_f32_32x32x16_bf16 v[2:17], v[2:5], v[6:9], 0
	s_waitcnt lgkmcnt(0)
	v_mfma_f32_32x32x16_bf16 v[2:17], v[100:103], v[108:111], v[2:17]
	global_load_dwordx4 v[100:103], v[44:45], off offset:96
	ds_read_b128 v[108:111], v98 offset:64
	ds_read_b128 v[112:115], v98 offset:96
	s_waitcnt vmcnt(1) lgkmcnt(1)
	v_mfma_f32_32x32x16_bf16 v[18:33], v[104:107], v[108:111], v[18:33]
	ds_read_b128 v[108:111], v98 offset:8768
	ds_read_b128 v[116:119], v98 offset:8800
	s_waitcnt lgkmcnt(1)
	v_mfma_f32_32x32x16_bf16 v[2:17], v[104:107], v[108:111], v[2:17]
	global_load_dwordx4 v[108:111], v[44:45], off offset:160
	v_mad_i64_i32 v[104:105], s[22:23], v128, s16, v[40:41]
	v_lshl_add_u64 v[124:125], v[104:105], 0, v[42:43]
	ds_read_b128 v[104:107], v98 offset:128
	v_add_co_u32_e32 v120, vcc, s17, v124
	s_waitcnt vmcnt(1)
	v_mfma_f32_32x32x16_bf16 v[18:33], v[100:103], v[112:115], v[18:33]
	ds_read_b128 v[112:115], v98 offset:160
	v_addc_co_u32_e32 v121, vcc, 0, v125, vcc
	s_waitcnt lgkmcnt(2)
	v_mfma_f32_32x32x16_bf16 v[2:17], v[100:103], v[116:119], v[2:17]
	global_load_dwordx4 v[100:103], v[44:45], off offset:128
	s_waitcnt vmcnt(0) lgkmcnt(1)
	v_mfma_f32_32x32x16_bf16 v[18:33], v[100:103], v[104:107], v[18:33]
	ds_read_b128 v[104:107], v98 offset:8832
	ds_read_b128 v[116:119], v98 offset:8864
	s_waitcnt lgkmcnt(1)
	v_mfma_f32_32x32x16_bf16 v[2:17], v[100:103], v[104:107], v[2:17]
	global_load_dwordx4 v[100:103], v[44:45], off offset:192
	global_load_dwordx4 v[104:107], v[44:45], off offset:224
	s_waitcnt vmcnt(0)
	v_mfma_f32_32x32x16_bf16 v[18:33], v[108:111], v[112:115], v[18:33]
	ds_read_b128 v[112:115], v98 offset:192
	ds_read_b128 v[120:123], v98 offset:224
	s_waitcnt lgkmcnt(1)
	v_mfma_f32_32x32x16_bf16 v[18:33], v[100:103], v[112:115], v[18:33]
	ds_read_b128 v[112:115], v98 offset:8896
	ds_read_b128 v[124:127], v98 offset:8928
	s_waitcnt lgkmcnt(2)
	v_mfma_f32_32x32x16_bf16 v[18:33], v[104:107], v[120:123], v[18:33]
	v_mfma_f32_32x32x16_bf16 v[2:17], v[108:111], v[116:119], v[2:17]
	s_waitcnt lgkmcnt(1)
	v_mfma_f32_32x32x16_bf16 v[2:17], v[100:103], v[112:115], v[2:17]
	s_waitcnt lgkmcnt(0)
	v_mfma_f32_32x32x16_bf16 v[2:17], v[104:107], v[124:127], v[2:17]
	s_mov_b32 s101, 0
	v_mad_i64_i32 v[100:101], s[22:23], v128, s16, v[40:41]
	v_and_b32_e32 v248, 3, v0
	v_mov_b32_e32 v251, 0
	v_mul_u32_u24_e32 v250, 0x53fe, v248
	v_lshl_add_u64 v[100:101], v[100:101], 0, v[42:43]
	v_ashrrev_i32_e32 v129, 31, v128
	v_lshl_add_u64 v[100:101], v[250:251], 0, v[100:101]
	v_lshlrev_b64 v[102:103], 11, v[128:129]
	v_lshl_add_u64 v[100:101], v[100:101], 0, s[10:11]
	v_lshl_add_u64 v[44:45], s[36:37], 0, v[42:43]
	v_mul_u32_u24_e32 v250, 0x7fe, v248
	v_lshl_add_u64 v[102:103], v[44:45], 0, v[102:103]
	v_lshl_add_u32 v249, v248, 2, v99
	v_lshl_add_u64 v[102:103], v[250:251], 0, v[102:103]
	global_load_dwordx2 v[104:105], v[100:101], off
	global_load_dwordx2 v[106:107], v[100:101], off offset:64
	global_load_dword v252, v249, s[0:1]
	s_mov_b32 s100, 0x2a000
	v_lshl_add_u64 v[122:123], v[100:101], 0, s[100:101]
	global_load_dwordx2 v[108:109], v[122:123], off
	global_load_dwordx2 v[110:111], v[122:123], off offset:64
	global_load_dword v253, v249, s[0:1] offset:32
	s_mov_b32 s100, 0x54000
	v_lshl_add_u64 v[122:123], v[100:101], 0, s[100:101]
	global_load_dwordx2 v[112:113], v[122:123], off
	global_load_dwordx2 v[114:115], v[122:123], off offset:64
	global_load_dword v254, v249, s[0:1] offset:64
	s_mov_b32 s100, 0x7e000
	v_lshl_add_u64 v[122:123], v[100:101], 0, s[100:101]
	global_load_dwordx2 v[116:117], v[122:123], off
	global_load_dwordx2 v[118:119], v[122:123], off offset:64
	global_load_dword v255, v249, s[0:1] offset:96
	s_mov_b32 vcc_lo, 0xaaaaaaaa
	s_mov_b32 vcc_hi, 0xaaaaaaaa
	s_nop 1
	v_mov_b32_e32 v120, v19
	v_mov_b32_e32 v121, v21
	v_mov_b32_e32 v124, v3
	v_mov_b32_e32 v125, v5
	v_cndmask_b32_dpp v19, v18, v19, vcc quad_perm:[1,0,3,2] row_mask:0xf bank_mask:0xf
	v_cndmask_b32_dpp v21, v20, v21, vcc quad_perm:[1,0,3,2] row_mask:0xf bank_mask:0xf
	v_cndmask_b32_dpp v3, v2, v3, vcc quad_perm:[1,0,3,2] row_mask:0xf bank_mask:0xf
	v_cndmask_b32_dpp v5, v4, v5, vcc quad_perm:[1,0,3,2] row_mask:0xf bank_mask:0xf
	s_mov_b32 vcc_lo, 0x55555555
	s_mov_b32 vcc_hi, 0x55555555
	s_nop 1
	v_cndmask_b32_dpp v18, v120, v18, vcc quad_perm:[1,0,3,2] row_mask:0xf bank_mask:0xf
	v_cndmask_b32_dpp v20, v121, v20, vcc quad_perm:[1,0,3,2] row_mask:0xf bank_mask:0xf
	v_cndmask_b32_dpp v2, v124, v2, vcc quad_perm:[1,0,3,2] row_mask:0xf bank_mask:0xf
	v_cndmask_b32_dpp v4, v125, v4, vcc quad_perm:[1,0,3,2] row_mask:0xf bank_mask:0xf
	s_mov_b32 vcc_lo, 0xcccccccc
	s_mov_b32 vcc_hi, 0xcccccccc
	s_nop 1
	v_mov_b32_e32 v120, v20
	v_mov_b32_e32 v121, v21
	v_mov_b32_e32 v124, v4
	v_mov_b32_e32 v125, v5
	v_cndmask_b32_dpp v20, v18, v20, vcc quad_perm:[2,3,0,1] row_mask:0xf bank_mask:0xf
	v_cndmask_b32_dpp v21, v19, v21, vcc quad_perm:[2,3,0,1] row_mask:0xf bank_mask:0xf
	v_cndmask_b32_dpp v4, v2, v4, vcc quad_perm:[2,3,0,1] row_mask:0xf bank_mask:0xf
	v_cndmask_b32_dpp v5, v3, v5, vcc quad_perm:[2,3,0,1] row_mask:0xf bank_mask:0xf
	s_mov_b32 vcc_lo, 0x33333333
	s_mov_b32 vcc_hi, 0x33333333
; __device__ __forceinline__ float bf2f(bf16_t b) { return __uint_as_float((unsigned)b << 16); }
; __device__ __forceinline__ bf16_t f2bf(float f) { return (bf16_t)(cvt_pk_bf16(f, 0.f) & 0xffffu); }
; __device__ __forceinline__ void gmlp_item(const bf16_t* __restrict__ proj, const epi::ss_t* __restrict__ ssv, const float* __restrict__ vgain, const bf16_t* __restrict__ wsb_l, const float* __restrict__ bs_l, ...
;     ...
;     for (int r = 0; r < 16; ++r) { const int q = 32 * qb + (r & 3) + 8 * (r >> 2) + 4 * hi, tok = tok0 + q; const float bq = bs_l[g * 128 + q];
;         const int c0 = g * 128 + 64 * ch + r32;
;         mlpo[(size_t)tok * 1024 + c0] = f2bf(bf2f(proj[(size_t)tok * NIN + C_ZU + c0]) * (a0[r] + bq));
;         mlpo[(size_t)tok * 1024 + c0 + 32] = f2bf(bf2f(proj[(size_t)tok * NIN + C_ZU + c0 + 32]) * (a1[r] + bq)); }
	s_nop 1
	v_cndmask_b32_dpp v18, v120, v18, vcc quad_perm:[2,3,0,1] row_mask:0xf bank_mask:0xf
	v_cndmask_b32_dpp v19, v121, v19, vcc quad_perm:[2,3,0,1] row_mask:0xf bank_mask:0xf
	v_cndmask_b32_dpp v2, v124, v2, vcc quad_perm:[2,3,0,1] row_mask:0xf bank_mask:0xf
	v_cndmask_b32_dpp v3, v125, v3, vcc quad_perm:[2,3,0,1] row_mask:0xf bank_mask:0xf
	s_mov_b32 vcc_lo, 0xaaaaaaaa
	s_mov_b32 vcc_hi, 0xaaaaaaaa
	s_nop 1
	v_mov_b32_e32 v120, v23
	v_mov_b32_e32 v121, v25
	v_mov_b32_e32 v124, v7
	v_mov_b32_e32 v125, v9
	v_cndmask_b32_dpp v23, v22, v23, vcc quad_perm:[1,0,3,2] row_mask:0xf bank_mask:0xf
	v_cndmask_b32_dpp v25, v24, v25, vcc quad_perm:[1,0,3,2] row_mask:0xf bank_mask:0xf
	v_cndmask_b32_dpp v7, v6, v7, vcc quad_perm:[1,0,3,2] row_mask:0xf bank_mask:0xf
	v_cndmask_b32_dpp v9, v8, v9, vcc quad_perm:[1,0,3,2] row_mask:0xf bank_mask:0xf
	s_mov_b32 vcc_lo, 0x55555555
	s_mov_b32 vcc_hi, 0x55555555
	s_nop 1
	v_cndmask_b32_dpp v22, v120, v22, vcc quad_perm:[1,0,3,2] row_mask:0xf bank_mask:0xf
	v_cndmask_b32_dpp v24, v121, v24, vcc quad_perm:[1,0,3,2] row_mask:0xf bank_mask:0xf
	v_cndmask_b32_dpp v6, v124, v6, vcc quad_perm:[1,0,3,2] row_mask:0xf bank_mask:0xf
	v_cndmask_b32_dpp v8, v125, v8, vcc quad_perm:[1,0,3,2] row_mask:0xf bank_mask:0xf
	s_mov_b32 vcc_lo, 0xcccccccc
	s_mov_b32 vcc_hi, 0xcccccccc
	s_nop 1
	v_mov_b32_e32 v120, v24
	v_mov_b32_e32 v121, v25
	v_mov_b32_e32 v124, v8
	v_mov_b32_e32 v125, v9
	v_cndmask_b32_dpp v24, v22, v24, vcc quad_perm:[2,3,0,1] row_mask:0xf bank_mask:0xf
	v_cndmask_b32_dpp v25, v23, v25, vcc quad_perm:[2,3,0,1] row_mask:0xf bank_mask:0xf
	v_cndmask_b32_dpp v8, v6, v8, vcc quad_perm:[2,3,0,1] row_mask:0xf bank_mask:0xf
	v_cndmask_b32_dpp v9, v7, v9, vcc quad_perm:[2,3,0,1] row_mask:0xf bank_mask:0xf
	s_mov_b32 vcc_lo, 0x33333333
	s_mov_b32 vcc_hi, 0x33333333
	s_nop 1
	v_cndmask_b32_dpp v22, v120, v22, vcc quad_perm:[2,3,0,1] row_mask:0xf bank_mask:0xf
	v_cndmask_b32_dpp v23, v121, v23, vcc quad_perm:[2,3,0,1] row_mask:0xf bank_mask:0xf
	v_cndmask_b32_dpp v6, v124, v6, vcc quad_perm:[2,3,0,1] row_mask:0xf bank_mask:0xf
	v_cndmask_b32_dpp v7, v125, v7, vcc quad_perm:[2,3,0,1] row_mask:0xf bank_mask:0xf
	s_mov_b32 vcc_lo, 0xaaaaaaaa
	s_mov_b32 vcc_hi, 0xaaaaaaaa
	s_nop 1
	v_mov_b32_e32 v120, v27
	v_mov_b32_e32 v121, v29
	v_mov_b32_e32 v124, v11
	v_mov_b32_e32 v125, v13
	v_cndmask_b32_dpp v27, v26, v27, vcc quad_perm:[1,0,3,2] row_mask:0xf bank_mask:0xf
	v_cndmask_b32_dpp v29, v28, v29, vcc quad_perm:[1,0,3,2] row_mask:0xf bank_mask:0xf
	v_cndmask_b32_dpp v11, v10, v11, vcc quad_perm:[1,0,3,2] row_mask:0xf bank_mask:0xf
	v_cndmask_b32_dpp v13, v12, v13, vcc quad_perm:[1,0,3,2] row_mask:0xf bank_mask:0xf
	s_mov_b32 vcc_lo, 0x55555555
	s_mov_b32 vcc_hi, 0x55555555
	s_nop 1
	v_cndmask_b32_dpp v26, v120, v26, vcc quad_perm:[1,0,3,2] row_mask:0xf bank_mask:0xf
	v_cndmask_b32_dpp v28, v121, v28, vcc quad_perm:[1,0,3,2] row_mask:0xf bank_mask:0xf
	v_cndmask_b32_dpp v10, v124, v10, vcc quad_perm:[1,0,3,2] row_mask:0xf bank_mask:0xf
	v_cndmask_b32_dpp v12, v125, v12, vcc quad_perm:[1,0,3,2] row_mask:0xf bank_mask:0xf
	s_mov_b32 vcc_lo, 0xcccccccc
	s_mov_b32 vcc_hi, 0xcccccccc
	s_nop 1
	v_mov_b32_e32 v120, v28
	v_mov_b32_e32 v121, v29
	v_mov_b32_e32 v124, v12
	v_mov_b32_e32 v125, v13
	v_cndmask_b32_dpp v28, v26, v28, vcc quad_perm:[2,3,0,1] row_mask:0xf bank_mask:0xf
	v_cndmask_b32_dpp v29, v27, v29, vcc quad_perm:[2,3,0,1] row_mask:0xf bank_mask:0xf
	v_cndmask_b32_dpp v12, v10, v12, vcc quad_perm:[2,3,0,1] row_mask:0xf bank_mask:0xf
	v_cndmask_b32_dpp v13, v11, v13, vcc quad_perm:[2,3,0,1] row_mask:0xf bank_mask:0xf
	s_mov_b32 vcc_lo, 0x33333333
	s_mov_b32 vcc_hi, 0x33333333
	s_nop 1
	v_cndmask_b32_dpp v26, v120, v26, vcc quad_perm:[2,3,0,1] row_mask:0xf bank_mask:0xf
	v_cndmask_b32_dpp v27, v121, v27, vcc quad_perm:[2,3,0,1] row_mask:0xf bank_mask:0xf
	v_cndmask_b32_dpp v10, v124, v10, vcc quad_perm:[2,3,0,1] row_mask:0xf bank_mask:0xf
	v_cndmask_b32_dpp v11, v125, v11, vcc quad_perm:[2,3,0,1] row_mask:0xf bank_mask:0xf
	s_mov_b32 vcc_lo, 0xaaaaaaaa
	s_mov_b32 vcc_hi, 0xaaaaaaaa
	s_nop 1
	v_mov_b32_e32 v120, v31
	v_mov_b32_e32 v121, v33
	v_mov_b32_e32 v124, v15
	v_mov_b32_e32 v125, v17
	v_cndmask_b32_dpp v31, v30, v31, vcc quad_perm:[1,0,3,2] row_mask:0xf bank_mask:0xf
	v_cndmask_b32_dpp v33, v32, v33, vcc quad_perm:[1,0,3,2] row_mask:0xf bank_mask:0xf
	v_cndmask_b32_dpp v15, v14, v15, vcc quad_perm:[1,0,3,2] row_mask:0xf bank_mask:0xf
	v_cndmask_b32_dpp v17, v16, v17, vcc quad_perm:[1,0,3,2] row_mask:0xf bank_mask:0xf
	s_mov_b32 vcc_lo, 0x55555555
	s_mov_b32 vcc_hi, 0x55555555
	s_nop 1
	v_cndmask_b32_dpp v30, v120, v30, vcc quad_perm:[1,0,3,2] row_mask:0xf bank_mask:0xf
	v_cndmask_b32_dpp v32, v121, v32, vcc quad_perm:[1,0,3,2] row_mask:0xf bank_mask:0xf
	v_cndmask_b32_dpp v14, v124, v14, vcc quad_perm:[1,0,3,2] row_mask:0xf bank_mask:0xf
	v_cndmask_b32_dpp v16, v125, v16, vcc quad_perm:[1,0,3,2] row_mask:0xf bank_mask:0xf
	s_mov_b32 vcc_lo, 0xcccccccc
	s_mov_b32 vcc_hi, 0xcccccccc
	s_nop 1
	v_mov_b32_e32 v120, v32
	v_mov_b32_e32 v121, v33
	v_mov_b32_e32 v124, v16
	v_mov_b32_e32 v125, v17
	v_cndmask_b32_dpp v32, v30, v32, vcc quad_perm:[2,3,0,1] row_mask:0xf bank_mask:0xf
	v_cndmask_b32_dpp v33, v31, v33, vcc quad_perm:[2,3,0,1] row_mask:0xf bank_mask:0xf
	v_cndmask_b32_dpp v16, v14, v16, vcc quad_perm:[2,3,0,1] row_mask:0xf bank_mask:0xf
	v_cndmask_b32_dpp v17, v15, v17, vcc quad_perm:[2,3,0,1] row_mask:0xf bank_mask:0xf
	s_mov_b32 vcc_lo, 0x33333333
	s_mov_b32 vcc_hi, 0x33333333
	s_nop 1
	v_cndmask_b32_dpp v30, v120, v30, vcc quad_perm:[2,3,0,1] row_mask:0xf bank_mask:0xf
	v_cndmask_b32_dpp v31, v121, v31, vcc quad_perm:[2,3,0,1] row_mask:0xf bank_mask:0xf
	v_cndmask_b32_dpp v14, v124, v14, vcc quad_perm:[2,3,0,1] row_mask:0xf bank_mask:0xf
	v_cndmask_b32_dpp v15, v125, v15, vcc quad_perm:[2,3,0,1] row_mask:0xf bank_mask:0xf
	s_waitcnt vmcnt(0)
; __device__ __forceinline__ float bf2f(bf16_t b) { return __uint_as_float((unsigned)b << 16); }
; __device__ __forceinline__ bf16_t f2bf(float f) { return (bf16_t)(cvt_pk_bf16(f, 0.f) & 0xffffu); }
; __device__ __forceinline__ void gmlp_item(const bf16_t* __restrict__ proj, const epi::ss_t* __restrict__ ssv, const float* __restrict__ vgain, const bf16_t* __restrict__ wsb_l, const float* __restrict__ bs_l, ...
;     ...
;     for (int r = 0; r < 16; ++r) { const int q = 32 * qb + (r & 3) + 8 * (r >> 2) + 4 * hi, tok = tok0 + q; const float bq = bs_l[g * 128 + q];
;         const int c0 = g * 128 + 64 * ch + r32;
;         mlpo[(size_t)tok * 1024 + c0] = f2bf(bf2f(proj[(size_t)tok * NIN + C_ZU + c0]) * (a0[r] + bq));
;         mlpo[(size_t)tok * 1024 + c0 + 32] = f2bf(bf2f(proj[(size_t)tok * NIN + C_ZU + c0 + 32]) * (a1[r] + bq)); }
;     __syncthreads();
	v_lshlrev_b32_e32 v120, 16, v104
	v_and_b32_e32 v121, 0xffff0000, v104
	v_lshlrev_b32_e32 v124, 16, v105
	v_and_b32_e32 v125, 0xffff0000, v105
	v_add_f32_e32 v18, v18, v252
	v_add_f32_e32 v19, v19, v252
	v_add_f32_e32 v20, v20, v252
	v_add_f32_e32 v21, v21, v252
	v_mul_f32_e32 v18, v18, v120
	v_mul_f32_e32 v19, v19, v121
	v_mul_f32_e32 v20, v20, v124
	v_mul_f32_e32 v21, v21, v125
	v_cvt_pk_bf16_f32 v18, v18, v19
	v_cvt_pk_bf16_f32 v19, v20, v21
	global_store_dwordx2 v[102:103], v[18:19], off
	v_lshlrev_b32_e32 v120, 16, v106
	v_and_b32_e32 v121, 0xffff0000, v106
	v_lshlrev_b32_e32 v124, 16, v107
	v_and_b32_e32 v125, 0xffff0000, v107
	v_add_f32_e32 v2, v2, v252
	v_add_f32_e32 v3, v3, v252
	v_add_f32_e32 v4, v4, v252
	v_add_f32_e32 v5, v5, v252
	v_mul_f32_e32 v2, v2, v120
	v_mul_f32_e32 v3, v3, v121
	v_mul_f32_e32 v4, v4, v124
	v_mul_f32_e32 v5, v5, v125
	v_cvt_pk_bf16_f32 v2, v2, v3
	v_cvt_pk_bf16_f32 v3, v4, v5
	global_store_dwordx2 v[102:103], v[2:3], off offset:64
	s_mov_b32 s100, 0x4000
	v_lshl_add_u64 v[122:123], v[102:103], 0, s[100:101]
	v_lshlrev_b32_e32 v120, 16, v108
	v_and_b32_e32 v121, 0xffff0000, v108
	v_lshlrev_b32_e32 v124, 16, v109
	v_and_b32_e32 v125, 0xffff0000, v109
	v_add_f32_e32 v22, v22, v253
	v_add_f32_e32 v23, v23, v253
	v_add_f32_e32 v24, v24, v253
	v_add_f32_e32 v25, v25, v253
	v_mul_f32_e32 v22, v22, v120
	v_mul_f32_e32 v23, v23, v121
	v_mul_f32_e32 v24, v24, v124
	v_mul_f32_e32 v25, v25, v125
	v_cvt_pk_bf16_f32 v22, v22, v23
	v_cvt_pk_bf16_f32 v23, v24, v25
	global_store_dwordx2 v[122:123], v[22:23], off
	v_lshlrev_b32_e32 v120, 16, v110
	v_and_b32_e32 v121, 0xffff0000, v110
	v_lshlrev_b32_e32 v124, 16, v111
	v_and_b32_e32 v125, 0xffff0000, v111
	v_add_f32_e32 v6, v6, v253
	v_add_f32_e32 v7, v7, v253
	v_add_f32_e32 v8, v8, v253
	v_add_f32_e32 v9, v9, v253
	v_mul_f32_e32 v6, v6, v120
	v_mul_f32_e32 v7, v7, v121
	v_mul_f32_e32 v8, v8, v124
	v_mul_f32_e32 v9, v9, v125
	v_cvt_pk_bf16_f32 v6, v6, v7
	v_cvt_pk_bf16_f32 v7, v8, v9
	global_store_dwordx2 v[122:123], v[6:7], off offset:64
	s_mov_b32 s100, 0x8000
	v_lshl_add_u64 v[122:123], v[102:103], 0, s[100:101]
	v_lshlrev_b32_e32 v120, 16, v112
	v_and_b32_e32 v121, 0xffff0000, v112
	v_lshlrev_b32_e32 v124, 16, v113
	v_and_b32_e32 v125, 0xffff0000, v113
	v_add_f32_e32 v26, v26, v254
	v_add_f32_e32 v27, v27, v254
	v_add_f32_e32 v28, v28, v254
	v_add_f32_e32 v29, v29, v254
	v_mul_f32_e32 v26, v26, v120
	v_mul_f32_e32 v27, v27, v121
	v_mul_f32_e32 v28, v28, v124
	v_mul_f32_e32 v29, v29, v125
	v_cvt_pk_bf16_f32 v26, v26, v27
	v_cvt_pk_bf16_f32 v27, v28, v29
	global_store_dwordx2 v[122:123], v[26:27], off
	v_lshlrev_b32_e32 v120, 16, v114
	v_and_b32_e32 v121, 0xffff0000, v114
	v_lshlrev_b32_e32 v124, 16, v115
	v_and_b32_e32 v125, 0xffff0000, v115
	v_add_f32_e32 v10, v10, v254
	v_add_f32_e32 v11, v11, v254
	v_add_f32_e32 v12, v12, v254
	v_add_f32_e32 v13, v13, v254
	v_mul_f32_e32 v10, v10, v120
	v_mul_f32_e32 v11, v11, v121
	v_mul_f32_e32 v12, v12, v124
	v_mul_f32_e32 v13, v13, v125
	v_cvt_pk_bf16_f32 v10, v10, v11
	v_cvt_pk_bf16_f32 v11, v12, v13
	global_store_dwordx2 v[122:123], v[10:11], off offset:64
	s_mov_b32 s100, 0xc000
	v_lshl_add_u64 v[122:123], v[102:103], 0, s[100:101]
	v_lshlrev_b32_e32 v120, 16, v116
	v_and_b32_e32 v121, 0xffff0000, v116
	v_lshlrev_b32_e32 v124, 16, v117
	v_and_b32_e32 v125, 0xffff0000, v117
	v_add_f32_e32 v30, v30, v255
	v_add_f32_e32 v31, v31, v255
	v_add_f32_e32 v32, v32, v255
	v_add_f32_e32 v33, v33, v255
	v_mul_f32_e32 v30, v30, v120
	v_mul_f32_e32 v31, v31, v121
	v_mul_f32_e32 v32, v32, v124
	v_mul_f32_e32 v33, v33, v125
	v_cvt_pk_bf16_f32 v30, v30, v31
	v_cvt_pk_bf16_f32 v31, v32, v33
	global_store_dwordx2 v[122:123], v[30:31], off
	v_lshlrev_b32_e32 v120, 16, v118
	v_and_b32_e32 v121, 0xffff0000, v118
	v_lshlrev_b32_e32 v124, 16, v119
	v_and_b32_e32 v125, 0xffff0000, v119
	v_add_f32_e32 v14, v14, v255
	v_add_f32_e32 v15, v15, v255
	v_add_f32_e32 v16, v16, v255
	v_add_f32_e32 v17, v17, v255
	v_mul_f32_e32 v14, v14, v120
	v_mul_f32_e32 v15, v15, v121
	v_mul_f32_e32 v16, v16, v124
	v_mul_f32_e32 v17, v17, v125
	v_cvt_pk_bf16_f32 v14, v14, v15
	v_cvt_pk_bf16_f32 v15, v16, v17
	global_store_dwordx2 v[122:123], v[14:15], off offset:64
	s_barrier
	s_cbranch_scc1 .LBB0_1629
